# attention row sums l through the matrix pipe: 4 extra 16x16x32 MFMAs (ones x P) per 64-key tile replace 32 v_add_f32 per lane and the cross-lane reduction; l now sums the bf16-rounded probabilities th
# speedup vs baseline: 1.0091x; 1.0058x over previous
; __device__ __forceinline__ int otid() { int t = threadIdx.x; asm volatile("" : "+v"(t)); return t; }
; __device__ __forceinline__ void attn_dma_body(const bf16_t* __restrict__ Qb, int ldq, int tpos0, const float* __restrict__ rope, const float* __restrict__ qgain, ...
;   const int tid = otid(), wid = tid >> 6, lane = tid & 63, r32 = lane & 31, hi = lane >> 5;
;   float* ws = (float*)(lds + TAB_OFF + 1024) + wid * 64; float* li_l = ws; float* al_l = ws + 32;
;   float m_reg = -1e30f, l_reg = 0; f32x16 o[4] = {}; bf16x8 qr[8];
;   const bf16_t* Qw = Qb + (long)(wid * QBLK + r32) * ldq + hi * 8;
;   unsigned koff[2], voff[2];
; #pragma unroll
;   for (int c = 0; c < 2; ++c) { const int g = c * 512 + tid;
;     { const int row = g >> 4, ch = (g & 15) ^ (row & 7); koff[c] = (unsigned)(row * 128 + ch * 8) * 2u; }
;     { const int sub = g >> 5, kk = (sub >> 2) * 8 + ((g >> 2) & 7), k = (kk & ~0xC) | ((kk & 4) << 1) | ((kk & 8) >> 1), col = (sub & 3) * 32 + (g & 3) * 8; voff[c] = (unsigned)(k * 128 + col) * 2u; } }
;   const unsigned wbase = (unsigned)__builtin_amdgcn_readfirstlane(wid) * 1024u;
;   typedef __attribute__((address_space(3))) unsigned lds_u32;
;   lds_u32* ldsl = (lds_u32*)(__attribute__((address_space(3))) char*)lds;
;     ...
;   const int NT = seq / KVBLK;
;   ATT_DMA(0, 0); ATT_DMA(1, 1);
; #pragma unroll
;   for (int d0 = 0; d0 < 8; ++d0) qr[d0] = ld8(Qw + d0 * 16);
;   if (tpos0 >= 0) {
;     float ss = 0.f;
; #pragma unroll
;     for (int d0 = 0; d0 < 8; ++d0)
; #pragma unroll
;       for (int i = 0; i < 8; ++i) { const float x = bf2f((unsigned)(unsigned short)qr[d0][i]); ss += x * x; }
;     { auto rr = __builtin_amdgcn_permlane32_swap(__float_as_uint(ss), __float_as_uint(ss), false, false); ss = __uint_as_float(rr[0]) + __uint_as_float(rr[1]); }
;     const float rinv = 1.0f / sqrtf(ss * (1.0f / 128.0f) + RMS_EPS);
;     const int t = tpos0 + wid * QBLK + r32;
; #pragma unroll
;     for (int ax = 0; ax < 2; ++ax) { const int pos = ax ? (t & 63) : (t >> 6);
; #pragma unroll
;       for (int q = 0; q < 2; ++q) { const int dl = 4 * ax + q, dh = dl + 2, p0 = q * 16 + 8 * hi;
;         const float* cp_ = rope + pos * 32 + p0; const float* gl = qgain + dl * 16 + 8 * hi; const float* gh = qgain + dh * 16 + 8 * hi;
;         float cs[8], sn[8], lo[8], hv[8];
; #pragma unroll
;         for (int i = 0; i < 8; ++i) { cs[i] = cp_[i]; sn[i] = cp_[4096 + i];
.LBB0_408:
	v_and_b32_e32 v167, 63, v147
	v_and_b32_e32 v246, 15, v167
	v_lshrrev_b32_e32 v247, 4, v167
	v_lshlrev_b32_e32 v248, 13, v179
	v_add_u32_e32 v248, 0x10000, v248
	v_lshl_add_u32 v249, v177, 8, v248
	v_lshl_add_u32 v249, v178, 4, v249
	ds_write_b128 v249, v[102:105] offset:0
	ds_write_b128 v249, v[110:113] offset:32
	ds_write_b128 v249, v[98:101] offset:64
	ds_write_b128 v249, v[106:109] offset:96
	ds_write_b128 v249, v[118:121] offset:128
	ds_write_b128 v249, v[126:129] offset:160
	ds_write_b128 v249, v[114:117] offset:192
	ds_write_b128 v249, v[122:125] offset:224
	v_lshl_add_u32 v251, v246, 8, v248
	v_lshl_add_u32 v251, v247, 4, v251
	s_waitcnt lgkmcnt(0)
	ds_read_b128 v[98:101], v251 offset:0
	ds_read_b128 v[102:105], v251 offset:64
	ds_read_b128 v[106:109], v251 offset:128
	ds_read_b128 v[110:113], v251 offset:192
	ds_read_b128 v[114:117], v251 offset:4096
	ds_read_b128 v[118:121], v251 offset:4160
	ds_read_b128 v[122:125], v251 offset:4224
	ds_read_b128 v[126:129], v251 offset:4288
	v_lshlrev_b32_e32 v252, 4, v246
	v_lshlrev_b32_e32 v253, 4, v247
	v_lshlrev_b32_e32 v254, 8, v246
	v_or_b32_e32 v255, 0, v253
	v_xor_b32_e32 v255, v255, v252
	v_or_b32_e32 v183, v255, v254
	v_or_b32_e32 v255, 64, v253
	v_xor_b32_e32 v255, v255, v252
	v_or_b32_e32 v184, v255, v254
	v_or_b32_e32 v255, 128, v253
	v_xor_b32_e32 v255, v255, v252
	v_or_b32_e32 v185, v255, v254
	v_or_b32_e32 v255, 192, v253
	v_xor_b32_e32 v255, v255, v252
	v_or_b32_e32 v186, v255, v254
	v_lshrrev_b32_e32 v252, 1, v247
	v_lshlrev_b32_e32 v252, 11, v252
	v_and_b32_e32 v253, 1, v247
	v_lshl_add_u32 v252, v253, 8, v252
	v_lshrrev_b32_e32 v254, 2, v246
	v_lshl_add_u32 v252, v254, 6, v252
	v_and_b32_e32 v254, 3, v246
	v_lshl_add_u32 v252, v254, 3, v252
	v_lshl_add_u32 v191, v253, 5, v252
	v_xor_b32_e32 v253, 1, v253
	v_lshl_add_u32 v192, v253, 5, v252
	v_add_u32_e32 v191, 0x4000, v191
	v_add_u32_e32 v192, 0x4000, v192
	v_readfirstlane_b32 s42, v179
	v_mov_b32_e32 v170, v162
	v_mov_b32_e32 v172, v32
	v_mov_b32_e32 v171, v30
	v_mov_b32_e32 v173, v34
	v_mov_b32_e32 v2, 0
	v_mov_b32_e32 v3, 0
	v_mov_b32_e32 v4, 0
	v_mov_b32_e32 v5, 0
	v_mov_b32_e32 v6, 0
	v_mov_b32_e32 v7, 0
	v_mov_b32_e32 v8, 0
	v_mov_b32_e32 v9, 0
	v_mov_b32_e32 v10, 0
	v_mov_b32_e32 v11, 0
	v_mov_b32_e32 v12, 0
	v_mov_b32_e32 v13, 0
	v_mov_b32_e32 v14, 0
	v_mov_b32_e32 v15, 0
	v_mov_b32_e32 v16, 0
	v_mov_b32_e32 v17, 0
	v_mov_b32_e32 v18, 0
	v_mov_b32_e32 v19, 0
	v_mov_b32_e32 v20, 0
	v_mov_b32_e32 v21, 0
	v_mov_b32_e32 v22, 0
	v_mov_b32_e32 v23, 0
	v_mov_b32_e32 v24, 0
	v_mov_b32_e32 v25, 0
	v_mov_b32_e32 v26, 0
	v_mov_b32_e32 v27, 0
	v_mov_b32_e32 v28, 0
	v_mov_b32_e32 v29, 0
	v_mov_b32_e32 v30, 0
	v_mov_b32_e32 v31, 0
	v_mov_b32_e32 v32, 0
	v_mov_b32_e32 v33, 0
	v_mov_b32_e32 v34, 0
	v_mov_b32_e32 v35, 0
	v_mov_b32_e32 v36, 0
	v_mov_b32_e32 v37, 0
	v_mov_b32_e32 v38, 0
	v_mov_b32_e32 v39, 0
	v_mov_b32_e32 v40, 0
	v_mov_b32_e32 v41, 0
	v_mov_b32_e32 v42, 0
	v_mov_b32_e32 v43, 0
	v_mov_b32_e32 v44, 0
	v_mov_b32_e32 v45, 0
	v_mov_b32_e32 v46, 0
	v_mov_b32_e32 v47, 0
	v_mov_b32_e32 v48, 0
	v_mov_b32_e32 v49, 0
	v_mov_b32_e32 v50, 0
	v_mov_b32_e32 v51, 0
	v_mov_b32_e32 v52, 0
	v_mov_b32_e32 v53, 0
	v_mov_b32_e32 v54, 0
	v_mov_b32_e32 v55, 0
	v_mov_b32_e32 v56, 0
	v_mov_b32_e32 v57, 0
	v_mov_b32_e32 v58, 0
	v_mov_b32_e32 v59, 0
	v_mov_b32_e32 v60, 0
	v_mov_b32_e32 v61, 0
	v_mov_b32_e32 v62, 0
	v_mov_b32_e32 v63, 0
	v_mov_b32_e32 v64, 0
	v_mov_b32_e32 v65, 0
	v_mov_b32_e32 v182, 0
	v_mov_b32_e32 v195, 0
	v_mov_b32_e32 v246, 0
	v_mov_b32_e32 v247, 0
	v_mov_b32_e32 v248, 0
	v_mov_b32_e32 v249, 0
	v_mov_b32_e32 v252, 0
	v_mov_b32_e32 v253, 0
	v_mov_b32_e32 v254, 0
	v_mov_b32_e32 v255, 0
	v_mov_b32_e32 v194, 0x3f803f80
	v_mov_b32_e32 v195, 0x3f803f80
	v_mov_b32_e32 v196, 0x3f803f80
	v_mov_b32_e32 v197, 0x3f803f80
	s_cmp_lt_u32 s42, 4
	s_cbranch_scc1 .Lf16_noprio
	s_setprio 1
.Lf16_noprio:
	s_waitcnt vmcnt(0) lgkmcnt(0)
	s_barrier
	s_add_u32 s2, s38, 0x8000
	s_addc_u32 s3, s39, 0
	s_add_u32 s4, s40, 0x8000
	s_addc_u32 s5, s41, 0
	s_add_i32 s6, s96, 0x10000
	s_mov_b32 m0, s6
	s_nop 0
	global_load_lds_dwordx4 v170, s[2:3]
	s_add_i32 m0, s6, 0x2000
	s_nop 0
	global_load_lds_dwordx4 v172, s[2:3]
	s_add_i32 m0, s6, 0x4000
	s_nop 0
	global_load_lds_dwordx4 v171, s[4:5]
	s_add_i32 m0, s6, 0x6000
	s_nop 0
	global_load_lds_dwordx4 v173, s[4:5]
	s_add_u32 s2, s2, 0x4000
	s_addc_u32 s3, s3, 0
	s_add_u32 s4, s4, 0x4000
	s_addc_u32 s5, s5, 0
	s_mov_b32 s36, 0
	v_add_u32_e32 v187, s36, v183
	v_add_u32_e32 v188, s36, v184
	v_add_u32_e32 v189, s36, v185
	v_add_u32_e32 v190, s36, v186
	ds_read_b128 v[146:149], v187 offset:0
	ds_read_b128 v[150:153], v187 offset:4096
	ds_read_b128 v[154:157], v187 offset:8192
	ds_read_b128 v[158:161], v187 offset:12288
	ds_read_b128 v[198:201], v188 offset:0
	ds_read_b128 v[202:205], v188 offset:4096
	ds_read_b128 v[206:209], v188 offset:8192
	ds_read_b128 v[210:213], v188 offset:12288
	s_waitcnt lgkmcnt(7)
	v_mfma_f32_16x16x32_bf16 v[66:69], v[146:149], v[98:101], 0
	v_mfma_f32_16x16x32_bf16 v[70:73], v[146:149], v[114:117], 0
	ds_read_b128 v[146:149], v189 offset:0
	s_waitcnt lgkmcnt(7)
	v_mfma_f32_16x16x32_bf16 v[74:77], v[150:153], v[98:101], 0
	v_mfma_f32_16x16x32_bf16 v[78:81], v[150:153], v[114:117], 0
	ds_read_b128 v[150:153], v189 offset:4096
	s_waitcnt lgkmcnt(7)
	v_mfma_f32_16x16x32_bf16 v[82:85], v[154:157], v[98:101], 0
	v_mfma_f32_16x16x32_bf16 v[86:89], v[154:157], v[114:117], 0
	ds_read_b128 v[154:157], v189 offset:8192
	s_waitcnt lgkmcnt(7)
	v_mfma_f32_16x16x32_bf16 v[90:93], v[158:161], v[98:101], 0
	v_mfma_f32_16x16x32_bf16 v[94:97], v[158:161], v[114:117], 0
	ds_read_b128 v[158:161], v189 offset:12288
	s_waitcnt lgkmcnt(7)
; #define SBAR() __builtin_amdgcn_sched_barrier(0)
; #define RESC(a) do { if (__any((a) < 1.f)) { if (hi == 0) al_l[r32] = (a); asm volatile("s_waitcnt lgkmcnt(0)" ::: "memory"); \
;     for (int d = 0; d < 4; ++d) for (int r = 0; r < 16; ++r) o[d][r] *= al_l[crow(r, hi)]; } } while (0)
; #define RESC(a) do { if (__any((a) < 1.f)) { if (hi == 0) al_l[r32] = (a); asm volatile("s_waitcnt lgkmcnt(0)" ::: "memory"); \
;     for (int d = 0; d < 4; ++d) for (int r = 0; r < 16; ++r) o[d][r] *= al_l[crow(r, hi)]; } } while (0)
; #define ATT_SYNC(jn) do { ATT_WAIT_BAR(); if ((jn) < NT) ATT_DMA((jn), (jn) & 3); } while (0)
; __device__ __forceinline__ void qkt(f32x16& p0, f32x16& p1, const bf16_t* Ks, const bf16x8* qr, int r32, int hi) {
;   p0 = f32x16{}; p1 = f32x16{};
;   for (int d0 = 0; d0 < 8; ++d0) { int cb = (d0 * 16 + hi * 8) * 2;
;     bf16x8 b0 = *reinterpret_cast<const bf16x8*>((const char*)Ks + KSWZ(r32, cb));
;     bf16x8 b1 = *reinterpret_cast<const bf16x8*>((const char*)Ks + KSWZ(32 + r32, cb));
;     p0 = __builtin_amdgcn_mfma_f32_32x32x16_bf16(b0, qr[d0], p0, 0, 0, 0);
;     p1 = __builtin_amdgcn_mfma_f32_32x32x16_bf16(b1, qr[d0], p1, 0, 0, 0); }
; }
; __device__ __forceinline__ void attn_dma_body(const bf16_t* __restrict__ Qb, int ldq, int tpos0, const float* __restrict__ rope, const float* __restrict__ qgain, ...
;     ...
;   qkt(pA0, pA1, (const bf16_t*)lds, qr, r32, hi); partialSM(pA0, pA1, m_reg, mnA, alA);
;   const bool lead = __builtin_amdgcn_readfirstlane(wid) < 4;
;     ...
;   for (int j = 1; j + 1 < NT; j += 2) {
;     { SBAR(); qkt(pB0, pB1, (const bf16_t*)(lds + (j & 3) * SHM_SLOT), qr, r32, hi);
;       finishSM(pA0, pA1, alA, l_reg, pa0, pa1, pa2, pa3); s16x4 va[8]; pv_rd<0>(va, vb0 + ((j - 1) & 3) * (int)SHM_SLOT); SBAR();
;       if (!lead) ATT_SYNC(j + 2);
;       pv_d0_pre(o, vb0 + ((j - 1) & 3) * (int)SHM_SLOT, va, pa0, pa1, pa2, pa3); partialSM(pB0, pB1, m_reg, mnB, alB);
;       if (lead) ATT_SYNC(j + 2);
;       RESC(alB); }
;     { SBAR(); qkt(pA0, pA1, (const bf16_t*)(lds + ((j + 1) & 3) * SHM_SLOT), qr, r32, hi);
	v_mfma_f32_16x16x32_bf16 v[66:69], v[198:201], v[102:105], v[66:69]
	v_mfma_f32_16x16x32_bf16 v[70:73], v[198:201], v[118:121], v[70:73]
	ds_read_b128 v[198:201], v190 offset:0
	s_waitcnt lgkmcnt(7)
	v_mfma_f32_16x16x32_bf16 v[74:77], v[202:205], v[102:105], v[74:77]
	v_mfma_f32_16x16x32_bf16 v[78:81], v[202:205], v[118:121], v[78:81]
	ds_read_b128 v[202:205], v190 offset:4096
	s_waitcnt lgkmcnt(7)
	v_mfma_f32_16x16x32_bf16 v[82:85], v[206:209], v[102:105], v[82:85]
	v_mfma_f32_16x16x32_bf16 v[86:89], v[206:209], v[118:121], v[86:89]
	ds_read_b128 v[206:209], v190 offset:8192
	s_waitcnt lgkmcnt(7)
	v_mfma_f32_16x16x32_bf16 v[90:93], v[210:213], v[102:105], v[90:93]
	v_mfma_f32_16x16x32_bf16 v[94:97], v[210:213], v[118:121], v[94:97]
	ds_read_b128 v[210:213], v190 offset:12288
	s_waitcnt lgkmcnt(7)
	v_mfma_f32_16x16x32_bf16 v[66:69], v[146:149], v[106:109], v[66:69]
	v_mfma_f32_16x16x32_bf16 v[70:73], v[146:149], v[122:125], v[70:73]
	s_waitcnt lgkmcnt(6)
	v_mfma_f32_16x16x32_bf16 v[74:77], v[150:153], v[106:109], v[74:77]
	v_mfma_f32_16x16x32_bf16 v[78:81], v[150:153], v[122:125], v[78:81]
	s_waitcnt lgkmcnt(5)
	v_mfma_f32_16x16x32_bf16 v[82:85], v[154:157], v[106:109], v[82:85]
	v_mfma_f32_16x16x32_bf16 v[86:89], v[154:157], v[122:125], v[86:89]
	s_waitcnt lgkmcnt(4)
	v_mfma_f32_16x16x32_bf16 v[90:93], v[158:161], v[106:109], v[90:93]
	v_mfma_f32_16x16x32_bf16 v[94:97], v[158:161], v[122:125], v[94:97]
	s_waitcnt lgkmcnt(3)
	v_mfma_f32_16x16x32_bf16 v[66:69], v[198:201], v[110:113], v[66:69]
	v_mfma_f32_16x16x32_bf16 v[70:73], v[198:201], v[126:129], v[70:73]
	s_waitcnt lgkmcnt(2)
	v_mfma_f32_16x16x32_bf16 v[74:77], v[202:205], v[110:113], v[74:77]
	v_mfma_f32_16x16x32_bf16 v[78:81], v[202:205], v[126:129], v[78:81]
	s_waitcnt lgkmcnt(1)
	v_mfma_f32_16x16x32_bf16 v[82:85], v[206:209], v[110:113], v[82:85]
	v_mfma_f32_16x16x32_bf16 v[86:89], v[206:209], v[126:129], v[86:89]
	s_waitcnt lgkmcnt(0)
	v_mfma_f32_16x16x32_bf16 v[90:93], v[210:213], v[110:113], v[90:93]
	v_mfma_f32_16x16x32_bf16 v[94:97], v[210:213], v[126:129], v[94:97]
	s_nop 7
	v_exp_f32_e32 v66, v66
	v_exp_f32_e32 v67, v67
	v_exp_f32_e32 v68, v68
	v_exp_f32_e32 v69, v69
	v_exp_f32_e32 v70, v70
	v_exp_f32_e32 v71, v71
	v_exp_f32_e32 v72, v72
	v_exp_f32_e32 v73, v73
	v_exp_f32_e32 v74, v74
	v_exp_f32_e32 v75, v75
	v_exp_f32_e32 v76, v76
	v_exp_f32_e32 v77, v77
	v_exp_f32_e32 v78, v78
	v_exp_f32_e32 v79, v79
	v_exp_f32_e32 v80, v80
	v_exp_f32_e32 v81, v81
	v_exp_f32_e32 v82, v82
	v_exp_f32_e32 v83, v83
	v_exp_f32_e32 v84, v84
	v_exp_f32_e32 v85, v85
	v_exp_f32_e32 v86, v86
	v_exp_f32_e32 v87, v87
	v_exp_f32_e32 v88, v88
	v_exp_f32_e32 v89, v89
	v_exp_f32_e32 v90, v90
	v_exp_f32_e32 v91, v91
	v_exp_f32_e32 v92, v92
	v_exp_f32_e32 v93, v93
	v_exp_f32_e32 v94, v94
	v_exp_f32_e32 v95, v95
	v_exp_f32_e32 v96, v96
	v_exp_f32_e32 v97, v97
	v_cvt_pk_bf16_f32 v130, v66, v67
	v_cvt_pk_bf16_f32 v131, v68, v69
	v_cvt_pk_bf16_f32 v132, v74, v75
	v_cvt_pk_bf16_f32 v133, v76, v77
	v_cvt_pk_bf16_f32 v134, v82, v83
	v_cvt_pk_bf16_f32 v135, v84, v85
	v_cvt_pk_bf16_f32 v136, v90, v91
	v_cvt_pk_bf16_f32 v137, v92, v93
	v_cvt_pk_bf16_f32 v138, v70, v71
	v_cvt_pk_bf16_f32 v139, v72, v73
	v_cvt_pk_bf16_f32 v140, v78, v79
	v_cvt_pk_bf16_f32 v141, v80, v81
	v_cvt_pk_bf16_f32 v142, v86, v87
	v_cvt_pk_bf16_f32 v143, v88, v89
	v_cvt_pk_bf16_f32 v144, v94, v95
	v_cvt_pk_bf16_f32 v145, v96, v97
	s_mov_b32 s97, 1
	.p2align 6
.Lf16_loop:
	s_lshl_b32 s36, s97, 15
	s_and_b32 s36, s36, 0x18000
	s_add_i32 s37, s36, 0x18000
	s_and_b32 s37, s37, 0x18000
	v_add_u32_e32 v187, s36, v183
	v_add_u32_e32 v188, s36, v184
	v_add_u32_e32 v189, s36, v185
	v_add_u32_e32 v190, s36, v186
	ds_read_b128 v[146:149], v187 offset:0
	ds_read_b128 v[150:153], v187 offset:4096
	ds_read_b128 v[154:157], v187 offset:8192
	ds_read_b128 v[158:161], v187 offset:12288
	ds_read_b128 v[198:201], v188 offset:0
	ds_read_b128 v[202:205], v188 offset:4096
	ds_read_b128 v[206:209], v188 offset:8192
	ds_read_b128 v[210:213], v188 offset:12288
	v_add_u32_e32 v180, s37, v191
	v_add_u32_e32 v181, s37, v192
	s_waitcnt lgkmcnt(7)
	v_mfma_f32_16x16x32_bf16 v[66:69], v[146:149], v[98:101], 0
	v_mfma_f32_16x16x32_bf16 v[70:73], v[146:149], v[114:117], 0
	ds_read_b128 v[146:149], v189 offset:0
	s_waitcnt lgkmcnt(7)
	v_mfma_f32_16x16x32_bf16 v[74:77], v[150:153], v[98:101], 0
	v_mfma_f32_16x16x32_bf16 v[78:81], v[150:153], v[114:117], 0
	ds_read_b128 v[150:153], v189 offset:4096
	s_waitcnt lgkmcnt(7)
	v_mfma_f32_16x16x32_bf16 v[82:85], v[154:157], v[98:101], 0
	v_mfma_f32_16x16x32_bf16 v[86:89], v[154:157], v[114:117], 0
	ds_read_b128 v[154:157], v189 offset:8192
	s_waitcnt lgkmcnt(7)
	v_mfma_f32_16x16x32_bf16 v[90:93], v[158:161], v[98:101], 0
	v_mfma_f32_16x16x32_bf16 v[94:97], v[158:161], v[114:117], 0
	ds_read_b128 v[158:161], v189 offset:12288
	s_waitcnt lgkmcnt(7)
	v_mfma_f32_16x16x32_bf16 v[66:69], v[198:201], v[102:105], v[66:69]
	v_mfma_f32_16x16x32_bf16 v[70:73], v[198:201], v[118:121], v[70:73]
	ds_read_b128 v[198:201], v190 offset:0
	s_waitcnt lgkmcnt(7)
	v_mfma_f32_16x16x32_bf16 v[74:77], v[202:205], v[102:105], v[74:77]
	v_mfma_f32_16x16x32_bf16 v[78:81], v[202:205], v[118:121], v[78:81]
	ds_read_b128 v[202:205], v190 offset:4096
	s_waitcnt lgkmcnt(7)
	v_mfma_f32_16x16x32_bf16 v[82:85], v[206:209], v[102:105], v[82:85]
	v_mfma_f32_16x16x32_bf16 v[86:89], v[206:209], v[118:121], v[86:89]
	ds_read_b128 v[206:209], v190 offset:8192
	s_waitcnt lgkmcnt(7)
	v_mfma_f32_16x16x32_bf16 v[90:93], v[210:213], v[102:105], v[90:93]
	v_mfma_f32_16x16x32_bf16 v[94:97], v[210:213], v[118:121], v[94:97]
	ds_read_b128 v[210:213], v190 offset:12288
	s_waitcnt lgkmcnt(7)
; #define SBAR() __builtin_amdgcn_sched_barrier(0)
; __device__ __forceinline__ void pv_d0(f32x16* o, int vb, bf16x8 pa0, bf16x8 pa1, bf16x8 pa2, bf16x8 pa3) {
;   s16x4 ra[8], rb[8];
;   pv_rd<0>(ra, vb); pv_rd<1>(rb, vb);
;   asm volatile("s_waitcnt lgkmcnt(8)" ::: "memory"); SBAR(); pv_mm(o[0], ra, pa0, pa1, pa2, pa3); pv_rd<2>(ra, vb);
;   asm volatile("s_waitcnt lgkmcnt(8)" ::: "memory"); SBAR(); pv_mm(o[1], rb, pa0, pa1, pa2, pa3); pv_rd<3>(rb, vb);
;   asm volatile("s_waitcnt lgkmcnt(8)" ::: "memory"); SBAR(); pv_mm(o[2], ra, pa0, pa1, pa2, pa3);
;   asm volatile("s_waitcnt lgkmcnt(0)" ::: "memory"); SBAR(); pv_mm(o[3], rb, pa0, pa1, pa2, pa3);
; }
; __device__ __forceinline__ void pv_d0_pre(f32x16* o, int vb, s16x4 (&ra)[8], bf16x8 pa0, bf16x8 pa1, bf16x8 pa2, bf16x8 pa3) {
;   s16x4 rb[8];
;   pv_rd<1>(rb, vb);
;   asm volatile("s_waitcnt lgkmcnt(8)" ::: "memory"); SBAR(); pv_mm(o[0], ra, pa0, pa1, pa2, pa3); pv_rd<2>(ra, vb);
;   asm volatile("s_waitcnt lgkmcnt(8)" ::: "memory"); SBAR(); pv_mm(o[1], rb, pa0, pa1, pa2, pa3); pv_rd<3>(rb, vb);
;   asm volatile("s_waitcnt lgkmcnt(8)" ::: "memory"); SBAR(); pv_mm(o[2], ra, pa0, pa1, pa2, pa3);
;   asm volatile("s_waitcnt lgkmcnt(0)" ::: "memory"); SBAR(); pv_mm(o[3], rb, pa0, pa1, pa2, pa3);
; }
; __device__ __forceinline__ void attn_dma_body(const bf16_t* __restrict__ Qb, int ldq, int tpos0, const float* __restrict__ rope, const float* __restrict__ qgain, ...
;     ...
;   for (int j = 1; j + 1 < NT; j += 2) {
;     { SBAR(); qkt(pB0, pB1, (const bf16_t*)(lds + (j & 3) * SHM_SLOT), qr, r32, hi);
;       finishSM(pA0, pA1, alA, l_reg, pa0, pa1, pa2, pa3); s16x4 va[8]; pv_rd<0>(va, vb0 + ((j - 1) & 3) * (int)SHM_SLOT); SBAR();
;       if (!lead) ATT_SYNC(j + 2);
;       pv_d0_pre(o, vb0 + ((j - 1) & 3) * (int)SHM_SLOT, va, pa0, pa1, pa2, pa3); partialSM(pB0, pB1, m_reg, mnB, alB);
;       if (lead) ATT_SYNC(j + 2);
;       RESC(alB); }
;     { SBAR(); qkt(pA0, pA1, (const bf16_t*)(lds + ((j + 1) & 3) * SHM_SLOT), qr, r32, hi);
;       finishSM(pB0, pB1, alB, l_reg, pa0, pa1, pa2, pa3); s16x4 va[8]; pv_rd<0>(va, vb0 + (j & 3) * (int)SHM_SLOT); SBAR();
;       if (!lead) ATT_SYNC(j + 3);
;       pv_d0_pre(o, vb0 + (j & 3) * (int)SHM_SLOT, va, pa0, pa1, pa2, pa3); partialSM(pA0, pA1, m_reg, mnA, alA);
;       if (lead) ATT_SYNC(j + 3);
;       RESC(alA); }
	v_mfma_f32_16x16x32_bf16 v[66:69], v[146:149], v[106:109], v[66:69]
	v_mfma_f32_16x16x32_bf16 v[70:73], v[146:149], v[122:125], v[70:73]
	s_waitcnt lgkmcnt(6)
	v_mfma_f32_16x16x32_bf16 v[74:77], v[150:153], v[106:109], v[74:77]
	v_mfma_f32_16x16x32_bf16 v[78:81], v[150:153], v[122:125], v[78:81]
	s_waitcnt lgkmcnt(5)
	v_mfma_f32_16x16x32_bf16 v[82:85], v[154:157], v[106:109], v[82:85]
	v_mfma_f32_16x16x32_bf16 v[86:89], v[154:157], v[122:125], v[86:89]
	s_waitcnt lgkmcnt(4)
	v_mfma_f32_16x16x32_bf16 v[90:93], v[158:161], v[106:109], v[90:93]
	v_mfma_f32_16x16x32_bf16 v[94:97], v[158:161], v[122:125], v[94:97]
	s_waitcnt lgkmcnt(3)
	v_mfma_f32_16x16x32_bf16 v[66:69], v[198:201], v[110:113], v[66:69]
	v_mfma_f32_16x16x32_bf16 v[70:73], v[198:201], v[126:129], v[70:73]
	ds_read_b64_tr_b16 v[214:215], v180 offset:0
	ds_read_b64_tr_b16 v[216:217], v180 offset:4096
	ds_read_b64_tr_b16 v[218:219], v181 offset:0
	ds_read_b64_tr_b16 v[220:221], v181 offset:4096
	ds_read_b64_tr_b16 v[222:223], v180 offset:512
	ds_read_b64_tr_b16 v[224:225], v180 offset:4608
	ds_read_b64_tr_b16 v[226:227], v181 offset:512
	ds_read_b64_tr_b16 v[228:229], v181 offset:4608
	s_waitcnt lgkmcnt(10)
	v_mfma_f32_16x16x32_bf16 v[74:77], v[202:205], v[110:113], v[74:77]
	v_mfma_f32_16x16x32_bf16 v[78:81], v[202:205], v[126:129], v[78:81]
	s_waitcnt lgkmcnt(9)
	v_mfma_f32_16x16x32_bf16 v[82:85], v[206:209], v[110:113], v[82:85]
	v_mfma_f32_16x16x32_bf16 v[86:89], v[206:209], v[126:129], v[86:89]
	s_waitcnt lgkmcnt(8)
	v_mfma_f32_16x16x32_bf16 v[90:93], v[210:213], v[110:113], v[90:93]
	v_mfma_f32_16x16x32_bf16 v[94:97], v[210:213], v[126:129], v[94:97]
	s_cmp_lt_u32 s42, 4
	s_cbranch_scc1 .Lf16_a
	s_cmp_ge_u32 s97, 131
	s_cbranch_scc1 .Lf16_se_nl
	s_waitcnt vmcnt(0) lgkmcnt(0)
	s_barrier
	s_cmp_ge_u32 s97, 130
	s_cbranch_scc1 .Lf16_se_nl
	s_add_i32 s6, s36, 0x10000
	s_and_b32 s6, s6, 0x18000
	s_add_i32 s6, s6, s96
	s_mov_b32 m0, s6
	s_nop 0
	global_load_lds_dwordx4 v170, s[2:3]
	s_add_i32 m0, s6, 0x2000
	s_nop 0
	global_load_lds_dwordx4 v172, s[2:3]
	s_add_i32 m0, s6, 0x4000
	s_nop 0
	global_load_lds_dwordx4 v171, s[4:5]
	s_add_i32 m0, s6, 0x6000
	s_nop 0
	global_load_lds_dwordx4 v173, s[4:5]
	s_add_u32 s2, s2, 0x4000
	s_addc_u32 s3, s3, 0
	s_add_u32 s4, s4, 0x4000
	s_addc_u32 s5, s5, 0
.Lf16_se_nl:
.Lf16_a:
	s_waitcnt lgkmcnt(6)
	v_mfma_f32_16x16x32_bf16 v[2:5], v[214:217], v[130:133], v[2:5]
	v_exp_f32_e32 v66, v66
	v_mfma_f32_16x16x32_bf16 v[6:9], v[214:217], v[138:141], v[6:9]
	v_exp_f32_e32 v67, v67
	ds_read_b64_tr_b16 v[230:231], v180 offset:1024
	ds_read_b64_tr_b16 v[232:233], v180 offset:5120
	s_waitcnt lgkmcnt(6)
	v_mfma_f32_16x16x32_bf16 v[10:13], v[218:221], v[130:133], v[10:13]
	v_exp_f32_e32 v68, v68
	v_mfma_f32_16x16x32_bf16 v[14:17], v[218:221], v[138:141], v[14:17]
	v_exp_f32_e32 v69, v69
	ds_read_b64_tr_b16 v[234:235], v181 offset:1024
	ds_read_b64_tr_b16 v[236:237], v181 offset:5120
	s_waitcnt lgkmcnt(6)
	v_mfma_f32_16x16x32_bf16 v[18:21], v[222:225], v[130:133], v[18:21]
	v_exp_f32_e32 v70, v70
	v_mfma_f32_16x16x32_bf16 v[22:25], v[222:225], v[138:141], v[22:25]
	v_exp_f32_e32 v71, v71
	ds_read_b64_tr_b16 v[238:239], v180 offset:1536
	ds_read_b64_tr_b16 v[240:241], v180 offset:5632
	s_waitcnt lgkmcnt(6)
	v_mfma_f32_16x16x32_bf16 v[26:29], v[226:229], v[130:133], v[26:29]
	v_exp_f32_e32 v72, v72
	v_mfma_f32_16x16x32_bf16 v[30:33], v[226:229], v[138:141], v[30:33]
	v_exp_f32_e32 v73, v73
	v_mfma_f32_16x16x32_bf16 v[246:249], v[194:197], v[130:133], v[246:249]
	ds_read_b64_tr_b16 v[242:243], v181 offset:1536
	ds_read_b64_tr_b16 v[244:245], v181 offset:5632
	s_waitcnt lgkmcnt(6)
	v_mfma_f32_16x16x32_bf16 v[34:37], v[230:233], v[130:133], v[34:37]
	v_exp_f32_e32 v74, v74
	v_mfma_f32_16x16x32_bf16 v[38:41], v[230:233], v[138:141], v[38:41]
	v_exp_f32_e32 v75, v75
	ds_read_b64_tr_b16 v[214:215], v180 offset:8192
	ds_read_b64_tr_b16 v[216:217], v180 offset:12288
	s_waitcnt lgkmcnt(6)
	v_mfma_f32_16x16x32_bf16 v[42:45], v[234:237], v[130:133], v[42:45]
	v_exp_f32_e32 v76, v76
	v_mfma_f32_16x16x32_bf16 v[46:49], v[234:237], v[138:141], v[46:49]
	v_exp_f32_e32 v77, v77
	ds_read_b64_tr_b16 v[218:219], v181 offset:8192
	ds_read_b64_tr_b16 v[220:221], v181 offset:12288
	s_waitcnt lgkmcnt(6)
	v_mfma_f32_16x16x32_bf16 v[50:53], v[238:241], v[130:133], v[50:53]
	v_exp_f32_e32 v78, v78
	v_mfma_f32_16x16x32_bf16 v[54:57], v[238:241], v[138:141], v[54:57]
	v_exp_f32_e32 v79, v79
	ds_read_b64_tr_b16 v[222:223], v180 offset:8704
	ds_read_b64_tr_b16 v[224:225], v180 offset:12800
	s_waitcnt lgkmcnt(6)
	v_mfma_f32_16x16x32_bf16 v[58:61], v[242:245], v[130:133], v[58:61]
	v_exp_f32_e32 v80, v80
	v_mfma_f32_16x16x32_bf16 v[62:65], v[242:245], v[138:141], v[62:65]
	v_exp_f32_e32 v81, v81
	v_mfma_f32_16x16x32_bf16 v[252:255], v[194:197], v[138:141], v[252:255]
	ds_read_b64_tr_b16 v[226:227], v181 offset:8704
	ds_read_b64_tr_b16 v[228:229], v181 offset:12800
	s_waitcnt lgkmcnt(6)
	v_mfma_f32_16x16x32_bf16 v[2:5], v[214:217], v[134:137], v[2:5]
	v_exp_f32_e32 v82, v82
	v_mfma_f32_16x16x32_bf16 v[6:9], v[214:217], v[142:145], v[6:9]
	v_exp_f32_e32 v83, v83
	ds_read_b64_tr_b16 v[230:231], v180 offset:9216
	ds_read_b64_tr_b16 v[232:233], v180 offset:13312
	s_waitcnt lgkmcnt(6)
	v_mfma_f32_16x16x32_bf16 v[10:13], v[218:221], v[134:137], v[10:13]
	v_exp_f32_e32 v84, v84
	v_mfma_f32_16x16x32_bf16 v[14:17], v[218:221], v[142:145], v[14:17]
	v_exp_f32_e32 v85, v85
	ds_read_b64_tr_b16 v[234:235], v181 offset:9216
	ds_read_b64_tr_b16 v[236:237], v181 offset:13312
	s_waitcnt lgkmcnt(6)
; #define SBAR() __builtin_amdgcn_sched_barrier(0)
; #define RESC(a) do { if (__any((a) < 1.f)) { if (hi == 0) al_l[r32] = (a); asm volatile("s_waitcnt lgkmcnt(0)" ::: "memory"); \
;     for (int d = 0; d < 4; ++d) for (int r = 0; r < 16; ++r) o[d][r] *= al_l[crow(r, hi)]; } } while (0)
; #define RESC(a) do { if (__any((a) < 1.f)) { if (hi == 0) al_l[r32] = (a); asm volatile("s_waitcnt lgkmcnt(0)" ::: "memory"); \
;     for (int d = 0; d < 4; ++d) for (int r = 0; r < 16; ++r) o[d][r] *= al_l[crow(r, hi)]; } } while (0)
; #define ATT_SYNC(jn) do { ATT_WAIT_BAR(); if ((jn) < NT) ATT_DMA((jn), (jn) & 3); } while (0)
; __device__ __forceinline__ void attn_dma_body(const bf16_t* __restrict__ Qb, int ldq, int tpos0, const float* __restrict__ rope, const float* __restrict__ qgain, ...
;     ...
;   for (int j = 1; j + 1 < NT; j += 2) {
;     { SBAR(); qkt(pB0, pB1, (const bf16_t*)(lds + (j & 3) * SHM_SLOT), qr, r32, hi);
;       finishSM(pA0, pA1, alA, l_reg, pa0, pa1, pa2, pa3); s16x4 va[8]; pv_rd<0>(va, vb0 + ((j - 1) & 3) * (int)SHM_SLOT); SBAR();
;       if (!lead) ATT_SYNC(j + 2);
;       pv_d0_pre(o, vb0 + ((j - 1) & 3) * (int)SHM_SLOT, va, pa0, pa1, pa2, pa3); partialSM(pB0, pB1, m_reg, mnB, alB);
;       if (lead) ATT_SYNC(j + 2);
;       RESC(alB); }
;     { SBAR(); qkt(pA0, pA1, (const bf16_t*)(lds + ((j + 1) & 3) * SHM_SLOT), qr, r32, hi);
;       finishSM(pB0, pB1, alB, l_reg, pa0, pa1, pa2, pa3); s16x4 va[8]; pv_rd<0>(va, vb0 + (j & 3) * (int)SHM_SLOT); SBAR();
;       if (!lead) ATT_SYNC(j + 3);
;       pv_d0_pre(o, vb0 + (j & 3) * (int)SHM_SLOT, va, pa0, pa1, pa2, pa3); partialSM(pA0, pA1, m_reg, mnA, alA);
;       if (lead) ATT_SYNC(j + 3);
;       RESC(alA); }
;   }
;     ...
;   { SBAR(); qkt(pB0, pB1, (const bf16_t*)(lds + ((NT - 1) & 3) * SHM_SLOT), qr, r32, hi);
;     finishSM(pA0, pA1, alA, l_reg, pa0, pa1, pa2, pa3); SBAR();
;     pv_d0(o, vb0 + ((NT - 2) & 3) * (int)SHM_SLOT, pa0, pa1, pa2, pa3); partialSM(pB0, pB1, m_reg, mnB, alB);
;     RESC(alB);
;     finishSM(pB0, pB1, alB, l_reg, pa0, pa1, pa2, pa3); SBAR();
;     pv_d0(o, vb0 + ((NT - 1) & 3) * (int)SHM_SLOT, pa0, pa1, pa2, pa3); }
	v_mfma_f32_16x16x32_bf16 v[18:21], v[222:225], v[134:137], v[18:21]
	v_exp_f32_e32 v86, v86
	v_mfma_f32_16x16x32_bf16 v[22:25], v[222:225], v[142:145], v[22:25]
	v_exp_f32_e32 v87, v87
	ds_read_b64_tr_b16 v[238:239], v180 offset:9728
	ds_read_b64_tr_b16 v[240:241], v180 offset:13824
	s_waitcnt lgkmcnt(6)
	v_mfma_f32_16x16x32_bf16 v[26:29], v[226:229], v[134:137], v[26:29]
	v_exp_f32_e32 v88, v88
	v_mfma_f32_16x16x32_bf16 v[30:33], v[226:229], v[142:145], v[30:33]
	v_exp_f32_e32 v89, v89
	v_mfma_f32_16x16x32_bf16 v[246:249], v[194:197], v[134:137], v[246:249]
	ds_read_b64_tr_b16 v[242:243], v181 offset:9728
	ds_read_b64_tr_b16 v[244:245], v181 offset:13824
	s_waitcnt lgkmcnt(6)
	v_mfma_f32_16x16x32_bf16 v[34:37], v[230:233], v[134:137], v[34:37]
	v_exp_f32_e32 v90, v90
	v_mfma_f32_16x16x32_bf16 v[38:41], v[230:233], v[142:145], v[38:41]
	v_exp_f32_e32 v91, v91
	s_waitcnt lgkmcnt(4)
	v_mfma_f32_16x16x32_bf16 v[42:45], v[234:237], v[134:137], v[42:45]
	v_exp_f32_e32 v92, v92
	v_mfma_f32_16x16x32_bf16 v[46:49], v[234:237], v[142:145], v[46:49]
	v_exp_f32_e32 v93, v93
	s_waitcnt lgkmcnt(2)
	v_mfma_f32_16x16x32_bf16 v[50:53], v[238:241], v[134:137], v[50:53]
	v_exp_f32_e32 v94, v94
	v_mfma_f32_16x16x32_bf16 v[54:57], v[238:241], v[142:145], v[54:57]
	v_exp_f32_e32 v95, v95
	s_waitcnt lgkmcnt(0)
	v_mfma_f32_16x16x32_bf16 v[58:61], v[242:245], v[134:137], v[58:61]
	v_exp_f32_e32 v96, v96
	v_mfma_f32_16x16x32_bf16 v[62:65], v[242:245], v[142:145], v[62:65]
	v_exp_f32_e32 v97, v97
	v_mfma_f32_16x16x32_bf16 v[252:255], v[194:197], v[142:145], v[252:255]
	s_cmp_lt_u32 s42, 4
	s_cbranch_scc0 .Lf16_b
	s_cmp_ge_u32 s97, 131
	s_cbranch_scc1 .Lf16_se_l
	s_waitcnt vmcnt(0) lgkmcnt(0)
	s_barrier
	s_cmp_ge_u32 s97, 130
	s_cbranch_scc1 .Lf16_se_l
	s_add_i32 s6, s36, 0x10000
	s_and_b32 s6, s6, 0x18000
	s_add_i32 s6, s6, s96
	s_mov_b32 m0, s6
	s_nop 0
	global_load_lds_dwordx4 v170, s[2:3]
	s_add_i32 m0, s6, 0x2000
	s_nop 0
	global_load_lds_dwordx4 v172, s[2:3]
	s_add_i32 m0, s6, 0x4000
	s_nop 0
	global_load_lds_dwordx4 v171, s[4:5]
	s_add_i32 m0, s6, 0x6000
	s_nop 0
	global_load_lds_dwordx4 v173, s[4:5]
	s_add_u32 s2, s2, 0x4000
	s_addc_u32 s3, s3, 0
	s_add_u32 s4, s4, 0x4000
	s_addc_u32 s5, s5, 0
.Lf16_se_l:
.Lf16_b:
	v_cvt_pk_bf16_f32 v130, v66, v67
	v_cvt_pk_bf16_f32 v131, v68, v69
	v_cvt_pk_bf16_f32 v132, v74, v75
	v_cvt_pk_bf16_f32 v133, v76, v77
	v_cvt_pk_bf16_f32 v134, v82, v83
	v_cvt_pk_bf16_f32 v135, v84, v85
	v_cvt_pk_bf16_f32 v136, v90, v91
	v_cvt_pk_bf16_f32 v137, v92, v93
	v_cvt_pk_bf16_f32 v138, v70, v71
	v_cvt_pk_bf16_f32 v139, v72, v73
	v_cvt_pk_bf16_f32 v140, v78, v79
	v_cvt_pk_bf16_f32 v141, v80, v81
	v_cvt_pk_bf16_f32 v142, v86, v87
	v_cvt_pk_bf16_f32 v143, v88, v89
	v_cvt_pk_bf16_f32 v144, v94, v95
	v_cvt_pk_bf16_f32 v145, v96, v97
	s_add_i32 s97, s97, 1
	s_cmp_lt_u32 s97, 132
	s_cbranch_scc1 .Lf16_loop
	s_mov_b32 s37, 0x18000
	v_add_u32_e32 v180, s37, v191
	v_add_u32_e32 v181, s37, v192
	ds_read_b64_tr_b16 v[214:215], v180 offset:0
	ds_read_b64_tr_b16 v[216:217], v180 offset:4096
	ds_read_b64_tr_b16 v[218:219], v181 offset:0
	ds_read_b64_tr_b16 v[220:221], v181 offset:4096
	ds_read_b64_tr_b16 v[222:223], v180 offset:512
	ds_read_b64_tr_b16 v[224:225], v180 offset:4608
	ds_read_b64_tr_b16 v[226:227], v181 offset:512
	ds_read_b64_tr_b16 v[228:229], v181 offset:4608
	s_waitcnt lgkmcnt(6)
	v_mfma_f32_16x16x32_bf16 v[2:5], v[214:217], v[130:133], v[2:5]
	v_mfma_f32_16x16x32_bf16 v[6:9], v[214:217], v[138:141], v[6:9]
	ds_read_b64_tr_b16 v[230:231], v180 offset:1024
	ds_read_b64_tr_b16 v[232:233], v180 offset:5120
	s_waitcnt lgkmcnt(6)
	v_mfma_f32_16x16x32_bf16 v[10:13], v[218:221], v[130:133], v[10:13]
	v_mfma_f32_16x16x32_bf16 v[14:17], v[218:221], v[138:141], v[14:17]
	ds_read_b64_tr_b16 v[234:235], v181 offset:1024
	ds_read_b64_tr_b16 v[236:237], v181 offset:5120
	s_waitcnt lgkmcnt(6)
	v_mfma_f32_16x16x32_bf16 v[18:21], v[222:225], v[130:133], v[18:21]
	v_mfma_f32_16x16x32_bf16 v[22:25], v[222:225], v[138:141], v[22:25]
	ds_read_b64_tr_b16 v[238:239], v180 offset:1536
	ds_read_b64_tr_b16 v[240:241], v180 offset:5632
	s_waitcnt lgkmcnt(6)
	v_mfma_f32_16x16x32_bf16 v[26:29], v[226:229], v[130:133], v[26:29]
	v_mfma_f32_16x16x32_bf16 v[30:33], v[226:229], v[138:141], v[30:33]
	v_mfma_f32_16x16x32_bf16 v[246:249], v[194:197], v[130:133], v[246:249]
	ds_read_b64_tr_b16 v[242:243], v181 offset:1536
	ds_read_b64_tr_b16 v[244:245], v181 offset:5632
	s_waitcnt lgkmcnt(6)
	v_mfma_f32_16x16x32_bf16 v[34:37], v[230:233], v[130:133], v[34:37]
	v_mfma_f32_16x16x32_bf16 v[38:41], v[230:233], v[138:141], v[38:41]
	ds_read_b64_tr_b16 v[214:215], v180 offset:8192
	ds_read_b64_tr_b16 v[216:217], v180 offset:12288
	s_waitcnt lgkmcnt(6)
	v_mfma_f32_16x16x32_bf16 v[42:45], v[234:237], v[130:133], v[42:45]
	v_mfma_f32_16x16x32_bf16 v[46:49], v[234:237], v[138:141], v[46:49]
	ds_read_b64_tr_b16 v[218:219], v181 offset:8192
	ds_read_b64_tr_b16 v[220:221], v181 offset:12288
	s_waitcnt lgkmcnt(6)
	v_mfma_f32_16x16x32_bf16 v[50:53], v[238:241], v[130:133], v[50:53]
	v_mfma_f32_16x16x32_bf16 v[54:57], v[238:241], v[138:141], v[54:57]
	ds_read_b64_tr_b16 v[222:223], v180 offset:8704
	ds_read_b64_tr_b16 v[224:225], v180 offset:12800
	s_waitcnt lgkmcnt(6)
	v_mfma_f32_16x16x32_bf16 v[58:61], v[242:245], v[130:133], v[58:61]
	v_mfma_f32_16x16x32_bf16 v[62:65], v[242:245], v[138:141], v[62:65]
	v_mfma_f32_16x16x32_bf16 v[252:255], v[194:197], v[138:141], v[252:255]
	ds_read_b64_tr_b16 v[226:227], v181 offset:8704
	ds_read_b64_tr_b16 v[228:229], v181 offset:12800
	s_waitcnt lgkmcnt(6)
; #define SBAR() __builtin_amdgcn_sched_barrier(0)
; __device__ __forceinline__ int crow(int r, int hi) { return (r & 3) + 8 * (r >> 2) + 4 * hi; }
; #define RESC(a) do { if (__any((a) < 1.f)) { if (hi == 0) al_l[r32] = (a); asm volatile("s_waitcnt lgkmcnt(0)" ::: "memory"); \
;     for (int d = 0; d < 4; ++d) for (int r = 0; r < 16; ++r) o[d][r] *= al_l[crow(r, hi)]; } } while (0)
; #define RESC(a) do { if (__any((a) < 1.f)) { if (hi == 0) al_l[r32] = (a); asm volatile("s_waitcnt lgkmcnt(0)" ::: "memory"); \
;     for (int d = 0; d < 4; ++d) for (int r = 0; r < 16; ++r) o[d][r] *= al_l[crow(r, hi)]; } } while (0)
; __device__ __forceinline__ void attn_dma_body(const bf16_t* __restrict__ Qb, int ldq, int tpos0, const float* __restrict__ rope, const float* __restrict__ qgain, ...
;     ...
;   { SBAR(); qkt(pB0, pB1, (const bf16_t*)(lds + ((NT - 1) & 3) * SHM_SLOT), qr, r32, hi);
;     finishSM(pA0, pA1, alA, l_reg, pa0, pa1, pa2, pa3); SBAR();
;     pv_d0(o, vb0 + ((NT - 2) & 3) * (int)SHM_SLOT, pa0, pa1, pa2, pa3); partialSM(pB0, pB1, m_reg, mnB, alB);
;     RESC(alB);
;     finishSM(pB0, pB1, alB, l_reg, pa0, pa1, pa2, pa3); SBAR();
;     pv_d0(o, vb0 + ((NT - 1) & 3) * (int)SHM_SLOT, pa0, pa1, pa2, pa3); }
;   if (hi == 0) li_l[r32] = l_reg; asm volatile("s_waitcnt lgkmcnt(0)" ::: "memory");
;   float rli[16];
; #pragma unroll
;   for (int r = 0; r < 16; ++r) rli[r] = __builtin_amdgcn_rcpf(li_l[crow(r, hi)]);
	v_mfma_f32_16x16x32_bf16 v[2:5], v[214:217], v[134:137], v[2:5]
	v_mfma_f32_16x16x32_bf16 v[6:9], v[214:217], v[142:145], v[6:9]
	ds_read_b64_tr_b16 v[230:231], v180 offset:9216
	ds_read_b64_tr_b16 v[232:233], v180 offset:13312
	s_waitcnt lgkmcnt(6)
	v_mfma_f32_16x16x32_bf16 v[10:13], v[218:221], v[134:137], v[10:13]
	v_mfma_f32_16x16x32_bf16 v[14:17], v[218:221], v[142:145], v[14:17]
	ds_read_b64_tr_b16 v[234:235], v181 offset:9216
	ds_read_b64_tr_b16 v[236:237], v181 offset:13312
	s_waitcnt lgkmcnt(6)
	v_mfma_f32_16x16x32_bf16 v[18:21], v[222:225], v[134:137], v[18:21]
	v_mfma_f32_16x16x32_bf16 v[22:25], v[222:225], v[142:145], v[22:25]
	ds_read_b64_tr_b16 v[238:239], v180 offset:9728
	ds_read_b64_tr_b16 v[240:241], v180 offset:13824
	s_waitcnt lgkmcnt(6)
	v_mfma_f32_16x16x32_bf16 v[26:29], v[226:229], v[134:137], v[26:29]
	v_mfma_f32_16x16x32_bf16 v[30:33], v[226:229], v[142:145], v[30:33]
	v_mfma_f32_16x16x32_bf16 v[246:249], v[194:197], v[134:137], v[246:249]
	ds_read_b64_tr_b16 v[242:243], v181 offset:9728
	ds_read_b64_tr_b16 v[244:245], v181 offset:13824
	s_waitcnt lgkmcnt(6)
	v_mfma_f32_16x16x32_bf16 v[34:37], v[230:233], v[134:137], v[34:37]
	v_mfma_f32_16x16x32_bf16 v[38:41], v[230:233], v[142:145], v[38:41]
	s_waitcnt lgkmcnt(4)
	v_mfma_f32_16x16x32_bf16 v[42:45], v[234:237], v[134:137], v[42:45]
	v_mfma_f32_16x16x32_bf16 v[46:49], v[234:237], v[142:145], v[46:49]
	s_waitcnt lgkmcnt(2)
	v_mfma_f32_16x16x32_bf16 v[50:53], v[238:241], v[134:137], v[50:53]
	v_mfma_f32_16x16x32_bf16 v[54:57], v[238:241], v[142:145], v[54:57]
	s_waitcnt lgkmcnt(0)
	v_mfma_f32_16x16x32_bf16 v[58:61], v[242:245], v[134:137], v[58:61]
	v_mfma_f32_16x16x32_bf16 v[62:65], v[242:245], v[142:145], v[62:65]
	v_mfma_f32_16x16x32_bf16 v[252:255], v[194:197], v[142:145], v[252:255]
	s_nop 7
	s_nop 7
	v_mov_b32_e32 v182, v246
	v_mov_b32_e32 v195, v252
	v_rcp_f32_e32 v182, v182
	v_rcp_f32_e32 v195, v195
	s_waitcnt lgkmcnt(0)
	s_barrier
; __device__ __forceinline__ unsigned f2bf(float f) { unsigned u = __builtin_bit_cast(unsigned, f); return (u + 0x7fffu + ((u >> 16) & 1u)) >> 16; }
; __device__ __forceinline__ int crow(int r, int hi) { return (r & 3) + 8 * (r >> 2) + 4 * hi; }
; #define ATT_WAIT_BAR() asm volatile("s_waitcnt vmcnt(0) lgkmcnt(0)\n\ts_barrier" ::: "memory")
; __device__ __forceinline__ void attn_dma_body(const bf16_t* __restrict__ Qb, int ldq, int tpos0, const float* __restrict__ rope, const float* __restrict__ qgain, ...
;     ...
;   if (hi == 0) li_l[r32] = l_reg; asm volatile("s_waitcnt lgkmcnt(0)" ::: "memory");
;   float rli[16];
; #pragma unroll
;   for (int r = 0; r < 16; ++r) rli[r] = __builtin_amdgcn_rcpf(li_l[crow(r, hi)]);
;   bf16_t* Ow = Ob + (long)(wid * QBLK) * LDO;
;   asm volatile("s_waitcnt lgkmcnt(0)\n\ts_barrier" ::: "memory");
;   { char* st = lds + wid * 8704;
; #pragma unroll
;     for (int r = 0; r < 16; ++r) { const int orow = crow(r, hi);
; #pragma unroll
;       for (int d0 = 0; d0 < 4; ++d0) *(bf16_t*)(st + orow * 272 + (d0 * 32 + r32) * 2) = (bf16_t)f2bf(o[d0][r] * rli[r]); }
;     asm volatile("s_waitcnt lgkmcnt(0)" ::: "memory");
; #pragma unroll
;     for (int i = 0; i < 8; ++i) { const int c = i * 64 + lane, row = c >> 4, cc = c & 15; const u32x4 v = *(const u32x4*)(st + row * 272 + cc * 16);
;       const bf16_t* gp = Ow + (long)row * LDO + cc * 8;
;       asm volatile("global_store_dwordx4 %0, %1, off sc1\n\ts_nop 1" :: "v"(gp), "v"(v) : "memory"); } }
;   ATT_WAIT_BAR();
	v_mul_u32_u24_e32 v84, 0x2200, v179
	v_and_b32_e32 v246, 15, v167
	v_lshrrev_b32_e32 v247, 4, v167
	v_mul_u32_u24_e32 v248, 0x110, v246
	v_add_u32_e32 v248, v248, v84
	v_lshl_add_u32 v248, v247, 3, v248
	v_mul_f32_e32 v2, v2, v182
	v_mul_f32_e32 v3, v3, v182
	v_mul_f32_e32 v4, v4, v182
	v_mul_f32_e32 v5, v5, v182
	v_cvt_pk_bf16_f32 v252, v2, v3
	v_cvt_pk_bf16_f32 v253, v4, v5
	ds_write_b64 v248, v[252:253] offset:0
	v_mul_f32_e32 v6, v6, v195
	v_mul_f32_e32 v7, v7, v195
	v_mul_f32_e32 v8, v8, v195
	v_mul_f32_e32 v9, v9, v195
	v_cvt_pk_bf16_f32 v254, v6, v7
	v_cvt_pk_bf16_f32 v255, v8, v9
	ds_write_b64 v248, v[254:255] offset:4352
	v_mul_f32_e32 v10, v10, v182
	v_mul_f32_e32 v11, v11, v182
	v_mul_f32_e32 v12, v12, v182
	v_mul_f32_e32 v13, v13, v182
	v_cvt_pk_bf16_f32 v252, v10, v11
	v_cvt_pk_bf16_f32 v253, v12, v13
	ds_write_b64 v248, v[252:253] offset:32
	v_mul_f32_e32 v14, v14, v195
	v_mul_f32_e32 v15, v15, v195
	v_mul_f32_e32 v16, v16, v195
	v_mul_f32_e32 v17, v17, v195
	v_cvt_pk_bf16_f32 v254, v14, v15
	v_cvt_pk_bf16_f32 v255, v16, v17
	ds_write_b64 v248, v[254:255] offset:4384
	v_mul_f32_e32 v18, v18, v182
	v_mul_f32_e32 v19, v19, v182
	v_mul_f32_e32 v20, v20, v182
	v_mul_f32_e32 v21, v21, v182
	v_cvt_pk_bf16_f32 v252, v18, v19
	v_cvt_pk_bf16_f32 v253, v20, v21
	ds_write_b64 v248, v[252:253] offset:64
	v_mul_f32_e32 v22, v22, v195
	v_mul_f32_e32 v23, v23, v195
	v_mul_f32_e32 v24, v24, v195
	v_mul_f32_e32 v25, v25, v195
	v_cvt_pk_bf16_f32 v254, v22, v23
	v_cvt_pk_bf16_f32 v255, v24, v25
	ds_write_b64 v248, v[254:255] offset:4416
	v_mul_f32_e32 v26, v26, v182
	v_mul_f32_e32 v27, v27, v182
	v_mul_f32_e32 v28, v28, v182
	v_mul_f32_e32 v29, v29, v182
	v_cvt_pk_bf16_f32 v252, v26, v27
	v_cvt_pk_bf16_f32 v253, v28, v29
	ds_write_b64 v248, v[252:253] offset:96
	v_mul_f32_e32 v30, v30, v195
	v_mul_f32_e32 v31, v31, v195
	v_mul_f32_e32 v32, v32, v195
	v_mul_f32_e32 v33, v33, v195
	v_cvt_pk_bf16_f32 v254, v30, v31
	v_cvt_pk_bf16_f32 v255, v32, v33
	ds_write_b64 v248, v[254:255] offset:4448
	v_mul_f32_e32 v34, v34, v182
	v_mul_f32_e32 v35, v35, v182
	v_mul_f32_e32 v36, v36, v182
	v_mul_f32_e32 v37, v37, v182
	v_cvt_pk_bf16_f32 v252, v34, v35
	v_cvt_pk_bf16_f32 v253, v36, v37
	ds_write_b64 v248, v[252:253] offset:128
	v_mul_f32_e32 v38, v38, v195
	v_mul_f32_e32 v39, v39, v195
	v_mul_f32_e32 v40, v40, v195
	v_mul_f32_e32 v41, v41, v195
	v_cvt_pk_bf16_f32 v254, v38, v39
	v_cvt_pk_bf16_f32 v255, v40, v41
	ds_write_b64 v248, v[254:255] offset:4480
	v_mul_f32_e32 v42, v42, v182
	v_mul_f32_e32 v43, v43, v182
	v_mul_f32_e32 v44, v44, v182
	v_mul_f32_e32 v45, v45, v182
	v_cvt_pk_bf16_f32 v252, v42, v43
	v_cvt_pk_bf16_f32 v253, v44, v45
	ds_write_b64 v248, v[252:253] offset:160
	v_mul_f32_e32 v46, v46, v195
	v_mul_f32_e32 v47, v47, v195
	v_mul_f32_e32 v48, v48, v195
	v_mul_f32_e32 v49, v49, v195
	v_cvt_pk_bf16_f32 v254, v46, v47
	v_cvt_pk_bf16_f32 v255, v48, v49
	ds_write_b64 v248, v[254:255] offset:4512
	v_mul_f32_e32 v50, v50, v182
	v_mul_f32_e32 v51, v51, v182
	v_mul_f32_e32 v52, v52, v182
	v_mul_f32_e32 v53, v53, v182
	v_cvt_pk_bf16_f32 v252, v50, v51
	v_cvt_pk_bf16_f32 v253, v52, v53
	ds_write_b64 v248, v[252:253] offset:192
	v_mul_f32_e32 v54, v54, v195
	v_mul_f32_e32 v55, v55, v195
	v_mul_f32_e32 v56, v56, v195
	v_mul_f32_e32 v57, v57, v195
	v_cvt_pk_bf16_f32 v254, v54, v55
	v_cvt_pk_bf16_f32 v255, v56, v57
	ds_write_b64 v248, v[254:255] offset:4544
	v_mul_f32_e32 v58, v58, v182
	v_mul_f32_e32 v59, v59, v182
	v_mul_f32_e32 v60, v60, v182
	v_mul_f32_e32 v61, v61, v182
	v_cvt_pk_bf16_f32 v252, v58, v59
	v_cvt_pk_bf16_f32 v253, v60, v61
	ds_write_b64 v248, v[252:253] offset:224
	v_mul_f32_e32 v62, v62, v195
	v_mul_f32_e32 v63, v63, v195
	v_mul_f32_e32 v64, v64, v195
	v_mul_f32_e32 v65, v65, v195
	v_cvt_pk_bf16_f32 v254, v62, v63
	v_cvt_pk_bf16_f32 v255, v64, v65
	ds_write_b64 v248, v[254:255] offset:4576
	s_waitcnt lgkmcnt(0)
	s_lshl_b64 s[6:7], s[70:71], 12
	s_add_u32 s6, s23, s6
	s_addc_u32 s7, s94, s7
	s_add_u32 s6, s6, s44
	s_addc_u32 s7, s7, s45
	v_ashrrev_i32_e32 v165, 31, v164
	v_lshlrev_b64 v[66:67], 12, v[164:165]
	v_lshl_add_u64 v[6:7], s[6:7], 0, v[66:67]
	v_lshlrev_b32_e32 v162, 4, v246
	v_lshl_add_u64 v[6:7], v[6:7], 0, v[162:163]
	v_lshlrev_b32_e32 v162, 12, v247
	v_lshl_add_u64 v[6:7], v[6:7], 0, v[162:163]
	v_mul_u32_u24_e32 v249, 0x110, v247
	v_add_u32_e32 v249, v249, v84
	v_lshl_add_u32 v249, v246, 4, v249
	ds_read_b128 v[10:13], v249 offset:0
	s_mov_b64 s[8:9], 0x0
	v_lshl_add_u64 v[8:9], v[6:7], 0, s[8:9]
	s_waitcnt lgkmcnt(0)
	global_store_dwordx4 v[8:9], v[10:13], off sc1
	s_nop 1
	ds_read_b128 v[14:17], v249 offset:1088
	s_mov_b64 s[8:9], 0x4000
	v_lshl_add_u64 v[8:9], v[6:7], 0, s[8:9]
	s_waitcnt lgkmcnt(0)
	global_store_dwordx4 v[8:9], v[14:17], off sc1
	s_nop 1
	ds_read_b128 v[10:13], v249 offset:2176
	s_mov_b64 s[8:9], 0x8000
	v_lshl_add_u64 v[8:9], v[6:7], 0, s[8:9]
	s_waitcnt lgkmcnt(0)
	global_store_dwordx4 v[8:9], v[10:13], off sc1
	s_nop 1
	ds_read_b128 v[14:17], v249 offset:3264
	s_mov_b64 s[8:9], 0xc000
	v_lshl_add_u64 v[8:9], v[6:7], 0, s[8:9]
	s_waitcnt lgkmcnt(0)
	global_store_dwordx4 v[8:9], v[14:17], off sc1
	s_nop 1
	ds_read_b128 v[10:13], v249 offset:4352
	s_mov_b64 s[8:9], 0x10000
	v_lshl_add_u64 v[8:9], v[6:7], 0, s[8:9]
	s_waitcnt lgkmcnt(0)
	global_store_dwordx4 v[8:9], v[10:13], off sc1
	s_nop 1
	ds_read_b128 v[14:17], v249 offset:5440
	s_mov_b64 s[8:9], 0x14000
	v_lshl_add_u64 v[8:9], v[6:7], 0, s[8:9]
	s_waitcnt lgkmcnt(0)
	global_store_dwordx4 v[8:9], v[14:17], off sc1
	s_nop 1
	ds_read_b128 v[10:13], v249 offset:6528
	s_mov_b64 s[8:9], 0x18000
	v_lshl_add_u64 v[8:9], v[6:7], 0, s[8:9]
	s_waitcnt lgkmcnt(0)
	global_store_dwordx4 v[8:9], v[10:13], off sc1
	s_nop 1
	ds_read_b128 v[14:17], v249 offset:7616
	s_mov_b64 s[8:9], 0x1c000
	v_lshl_add_u64 v[8:9], v[6:7], 0, s[8:9]
	s_waitcnt lgkmcnt(0)
	global_store_dwordx4 v[8:9], v[14:17], off sc1
	s_nop 1
	s_waitcnt vmcnt(0) lgkmcnt(0)
	s_barrier
	v_readlane_b32 s96, v250, 4
	v_readlane_b32 s97, v250, 5
	s_setprio 0
	s_branch .LBB0_437
